# grid barrier release: last arriver bumps every XCD generation word directly
# speedup vs baseline: 1.0164x; 1.0050x over previous
.LBB0_168:
	s_or_b64 exec, exec, s[12:13]
	s_and_saveexec_b64 s[8:9], s[16:17]
	s_cbranch_execz .LBB0_170
	v_mov_b32_e32 v1, 1
	global_atomic_add v[2:3], v1, off
	s_mov_b32 s98, 0xffffef00
	s_mov_b32 s99, -1
	v_lshl_add_u64 v[2:3], v[2:3], 0, s[98:99]
	global_atomic_add v[2:3], v1, off
	global_atomic_add v[2:3], v1, off offset:256
	global_atomic_add v[2:3], v1, off offset:512
	global_atomic_add v[2:3], v1, off offset:768
	global_atomic_add v[2:3], v1, off offset:1024
	global_atomic_add v[2:3], v1, off offset:1280
	global_atomic_add v[2:3], v1, off offset:1536
	global_atomic_add v[2:3], v1, off offset:1792
	global_atomic_add v[2:3], v1, off offset:2048
	global_atomic_add v[2:3], v1, off offset:2304
	global_atomic_add v[2:3], v1, off offset:2560
	global_atomic_add v[2:3], v1, off offset:2816
	global_atomic_add v[2:3], v1, off offset:3072
	global_atomic_add v[2:3], v1, off offset:3328
	global_atomic_add v[2:3], v1, off offset:3584
	global_atomic_add v[2:3], v1, off offset:3840
.LBB0_170:
	s_or_b64 exec, exec, s[8:9]
	v_mov_b32_e32 v1, 0x2000
	v_mov_b32_e32 v2, 1
	s_waitcnt vmcnt(0)
	s_waitcnt vmcnt(0)

.LBB0_222:
	s_or_b64 exec, exec, s[10:11]
	s_and_saveexec_b64 s[8:9], s[14:15]
	s_cbranch_execz .LBB0_224
	v_mov_b32_e32 v1, 1
	global_atomic_add v[2:3], v1, off
	s_mov_b32 s98, 0xffffef00
	s_mov_b32 s99, -1
	v_lshl_add_u64 v[2:3], v[2:3], 0, s[98:99]
	global_atomic_add v[2:3], v1, off
	global_atomic_add v[2:3], v1, off offset:256
	global_atomic_add v[2:3], v1, off offset:512
	global_atomic_add v[2:3], v1, off offset:768
	global_atomic_add v[2:3], v1, off offset:1024
	global_atomic_add v[2:3], v1, off offset:1280
	global_atomic_add v[2:3], v1, off offset:1536
	global_atomic_add v[2:3], v1, off offset:1792
	global_atomic_add v[2:3], v1, off offset:2048
	global_atomic_add v[2:3], v1, off offset:2304
	global_atomic_add v[2:3], v1, off offset:2560
	global_atomic_add v[2:3], v1, off offset:2816
	global_atomic_add v[2:3], v1, off offset:3072
	global_atomic_add v[2:3], v1, off offset:3328
	global_atomic_add v[2:3], v1, off offset:3584
	global_atomic_add v[2:3], v1, off offset:3840

.LBB0_3059:
	s_or_b64 exec, exec, s[8:9]
	s_and_saveexec_b64 s[6:7], s[12:13]
	s_cbranch_execz .LBB0_3061
	v_mov_b32_e32 v2, 1
	global_atomic_add v[0:1], v2, off
	s_mov_b32 s98, 0xffffef00
	s_mov_b32 s99, -1
	v_lshl_add_u64 v[0:1], v[0:1], 0, s[98:99]
	global_atomic_add v[0:1], v2, off
	global_atomic_add v[0:1], v2, off offset:256
	global_atomic_add v[0:1], v2, off offset:512
	global_atomic_add v[0:1], v2, off offset:768
	global_atomic_add v[0:1], v2, off offset:1024
	global_atomic_add v[0:1], v2, off offset:1280
	global_atomic_add v[0:1], v2, off offset:1536
	global_atomic_add v[0:1], v2, off offset:1792
	global_atomic_add v[0:1], v2, off offset:2048
	global_atomic_add v[0:1], v2, off offset:2304
	global_atomic_add v[0:1], v2, off offset:2560
	global_atomic_add v[0:1], v2, off offset:2816
	global_atomic_add v[0:1], v2, off offset:3072
	global_atomic_add v[0:1], v2, off offset:3328
	global_atomic_add v[0:1], v2, off offset:3584
	global_atomic_add v[0:1], v2, off offset:3840
.LBB0_3061:
	s_or_b64 exec, exec, s[6:7]
	v_mov_b32_e32 v0, 0x2000
	v_mov_b32_e32 v1, 1
	s_waitcnt vmcnt(0)
	s_waitcnt vmcnt(0)
